# P4 key-loop cross-half max and P11b EpiDown per-row-group absmax via v_permlane16/32_swap instead of ds_bpermute round trips; on top of v68
# speedup vs baseline: 1.0131x; 1.0102x over previous
; #define LAS __attribute__((address_space(3)))
; DI int crow(int i, int h) { return (i & 3) + 8 * (i >> 2) + 4 * h; }
; #define MFMA32(a, b, c) __builtin_amdgcn_mfma_f32_32x32x16_bf16((a), (b), (c), 0, 0, 0)
; DI void attn_unit(LAS unsigned char* ldsb, const bf16* proj, const bf16* KR, const bf16* VTg, const float* rope, const float* sinks, unsigned char* yab, int kvh, int ab) {
;     ...
;         for (int kt = 0; kt < 17; ++kt) {
;             const bool lat = kt >= 8; const int j = kt - 8, T = Tq + j, kb = kb0 + 32 * j, slot = (T + 2 * NSLOT) % NSLOT;
;             if (lat && (T < 0 || T >= NTOK / 32)) continue;
;             const LAS unsigned char* Kb = lat ? KL + (32 * slot + r) * KRS : KC + (32 * kt + r) * KRS;
;             const LAS unsigned char* Vb = lat ? VL + r * VLRS + 64 * slot : VC + r * VCRS + 64 * kt;
;             const int vrs32 = 32 * (lat ? VLRS : VCRS); const bool edge = lat && (j == 0 || j == 8);
;             f32x16 s;
; #pragma unroll
;             for (int i = 0; i < 16; ++i) s[i] = 0.f;
; #pragma unroll
;             for (int ks = 0; ks < 4; ++ks) { const bf16x8 kf = *(const LAS bf16x8*)(Kb + (16 * ks + 8 * h5) * 2); s = MFMA32(kf, qf[ks], s); }
;             float mt = -INFINITY;
; #pragma unroll
;             for (int i = 0; i < 16; ++i) { float v = s[i];
;                 if (edge) { const int dk = kb + crow(i, h5) - qp; if (dk > 128 || dk < -128) v = -INFINITY; }
;                 s[i] = v; mt = fmaxf(mt, v); }
;             mt = fmaxf(mt, __shfl_xor(mt, 32));
;             if (__any(mt > m_run + 8.0f)) { const float mn = fmaxf(m_run, mt); const float alpha = __builtin_amdgcn_exp2f(m_run - mn); l_run *= alpha; m_run = mn;
; #pragma unroll
;                 for (int i = 0; i < 16; ++i) { o0[i] *= alpha; o1[i] *= alpha; } }
.LBB0_1312:
	s_cmp_gt_u32 s55, 7
	s_cselect_b64 s[4:5], -1, 0
	s_add_i32 s6, s65, s55
	s_add_i32 s6, s6, -12
	s_cmpk_gt_u32 s6, 0x1ff
	s_cselect_b64 s[6:7], -1, 0
	s_and_b64 s[6:7], s[4:5], s[6:7]
	s_and_b64 vcc, exec, s[6:7]
	s_cbranch_vccnz .LBB0_1311
	s_mul_hi_u32 s6, s54, 0xcccccccd
	s_lshr_b32 s71, s6, 3
	s_mul_i32 s6, s71, 10
	s_sub_i32 s6, s35, s6
	s_add_i32 s72, s55, -8
	s_add_i32 s8, s55, s6
	s_and_b64 s[6:7], s[4:5], exec
	s_cselect_b32 s6, s8, s55
	v_lshl_or_b32 v3, s6, 5, v1
	s_cselect_b32 s7, s3, 0
	v_mul_lo_u32 v3, v3, s45
	v_add3_u32 v3, s7, v3, v92
	ds_read_b128 v[36:39], v3
	ds_read_b128 v[180:183], v3 offset:32
	ds_read_b128 v[184:187], v3 offset:64
	s_waitcnt lgkmcnt(2)
	v_mfma_f32_32x32x16_bf16 v[36:51], v[36:39], v[72:75], 0
	s_and_b32 s72, s72, -9
	v_add_u32_e32 v188, s24, v169
	s_cmp_eq_u32 s72, 0
	v_add_u32_e32 v179, 0xfffffdff, v188
	s_cselect_b64 s[72:73], -1, 0
	v_add_u32_e32 v189, 0xfffffe00, v188
	v_cmp_gt_u32_e32 vcc, s59, v179
	s_waitcnt lgkmcnt(1)
	v_mfma_f32_32x32x16_bf16 v[36:51], v[180:183], v[80:83], v[36:51]
	ds_read_b128 v[180:183], v3 offset:96
	s_and_b64 s[72:73], s[4:5], s[72:73]
	v_add_u32_e32 v190, 0xfffffe01, v188
	v_cmp_gt_u32_e64 s[6:7], s59, v189
	s_and_b64 vcc, s[72:73], vcc
	v_add_u32_e32 v191, 0xfffffe02, v188
	v_cmp_gt_u32_e64 s[8:9], s59, v190
	s_waitcnt lgkmcnt(1)
	v_mfma_f32_32x32x16_bf16 v[36:51], v[184:187], v[76:79], v[36:51]
	v_add_u32_e32 v192, 0xfffffe07, v188
	v_cmp_gt_u32_e64 s[10:11], s59, v191
	v_add_u32_e32 v193, 0xfffffe08, v188
	v_cmp_gt_u32_e64 s[12:13], s59, v192
	v_add_u32_e32 v194, 0xfffffe09, v188
	v_cmp_gt_u32_e64 s[14:15], s59, v193
	v_cmp_gt_u32_e64 s[16:17], s59, v194
	s_waitcnt lgkmcnt(0)
	v_mfma_f32_32x32x16_bf16 v[36:51], v[180:183], v[84:87], v[36:51]
	s_nop 11
	v_cndmask_b32_e32 v183, v36, v172, vcc
	s_and_b64 vcc, s[72:73], s[6:7]
	v_cndmask_b32_e32 v182, v37, v172, vcc
	s_and_b64 vcc, s[72:73], s[8:9]
	v_cndmask_b32_e32 v181, v38, v172, vcc
	s_and_b64 vcc, s[72:73], s[10:11]
	v_cndmask_b32_e32 v180, v39, v172, vcc
	s_and_b64 vcc, s[72:73], s[12:13]
	v_cndmask_b32_e32 v179, v40, v172, vcc
	s_and_b64 vcc, s[72:73], s[14:15]
	v_cndmask_b32_e32 v40, v41, v172, vcc
	s_and_b64 vcc, s[72:73], s[16:17]
	v_add_u32_e32 v36, 0xfffffe0a, v188
	v_cndmask_b32_e32 v41, v42, v172, vcc
	v_cmp_gt_u32_e32 vcc, s59, v36
	s_and_b64 vcc, s[72:73], vcc
	v_add_u32_e32 v36, 0xfffffe0f, v188
	v_cndmask_b32_e32 v42, v43, v172, vcc
	v_cmp_gt_u32_e32 vcc, s59, v36
	s_and_b64 vcc, s[72:73], vcc
	v_add_u32_e32 v36, 0xfffffe10, v188
	v_cndmask_b32_e32 v44, v44, v172, vcc
	v_cmp_gt_u32_e32 vcc, s59, v36
	s_and_b64 vcc, s[72:73], vcc
	v_add_u32_e32 v36, 0xfffffe11, v188
	v_max3_f32 v3, v183, s61, v182
	v_cndmask_b32_e32 v43, v45, v172, vcc
	v_cmp_gt_u32_e32 vcc, s59, v36
	v_max3_f32 v3, v3, v181, v180
	s_and_b64 vcc, s[72:73], vcc
	v_add_u32_e32 v36, 0xfffffe12, v188
	v_max3_f32 v3, v3, v179, v40
	v_cndmask_b32_e32 v45, v46, v172, vcc
	v_cmp_gt_u32_e32 vcc, s59, v36
	v_max3_f32 v3, v3, v41, v42
	s_and_b64 vcc, s[72:73], vcc
	v_max3_f32 v3, v3, v44, v43
	v_cndmask_b32_e32 v39, v47, v172, vcc
	v_max3_f32 v37, v3, v45, v39
	v_add_u32_e32 v3, 0xfffffe17, v188
	v_cmp_gt_u32_e32 vcc, s59, v3
	s_and_b64 vcc, s[72:73], vcc
	v_add_u32_e32 v36, 0xfffffe18, v188
	v_cndmask_b32_e32 v3, v48, v172, vcc
	v_cmp_gt_u32_e32 vcc, s59, v36
	s_and_b64 vcc, s[72:73], vcc
	s_nop 0
	v_cndmask_b32_e32 v36, v49, v172, vcc
	v_max3_f32 v46, v37, v3, v36
	v_add_u32_e32 v37, 0xfffffe19, v188
	v_cmp_gt_u32_e32 vcc, s59, v37
	s_and_b64 vcc, s[72:73], vcc
	v_add_u32_e32 v37, 0xfffffe1a, v188
	v_cndmask_b32_e32 v38, v50, v172, vcc
	v_cmp_gt_u32_e32 vcc, s59, v37
	s_and_b64 vcc, s[72:73], vcc
	s_nop 0
	v_cndmask_b32_e32 v37, v51, v172, vcc
	v_max3_f32 v46, v46, v38, v37
	v_mov_b32_e32 v47, v46
	s_waitcnt lgkmcnt(0)
	s_nop 0
	v_permlane32_swap_b32 v46, v47
	v_max_f32_e32 v46, v46, v47
	v_add_f32_e32 v47, 0x41000000, v178
	v_cmp_gt_f32_e32 vcc, v46, v47
	s_cbranch_vccz .LBB0_1310
	v_max_f32_e32 v46, v46, v46
	v_max_f32_e32 v47, v178, v178
	v_max_f32_e32 v47, v47, v46
	v_sub_f32_e32 v46, v178, v47
	v_exp_f32_e32 v46, v46
	v_mov_b32_e32 v178, v47
	v_pk_mul_f32 v[34:35], v[34:35], v[46:47] op_sel_hi:[1,0]
	v_pk_mul_f32 v[32:33], v[32:33], v[46:47] op_sel_hi:[1,0]
	v_pk_mul_f32 v[30:31], v[30:31], v[46:47] op_sel_hi:[1,0]
	v_pk_mul_f32 v[28:29], v[28:29], v[46:47] op_sel_hi:[1,0]
	v_pk_mul_f32 v[26:27], v[26:27], v[46:47] op_sel_hi:[1,0]
	v_pk_mul_f32 v[24:25], v[24:25], v[46:47] op_sel_hi:[1,0]
	v_pk_mul_f32 v[22:23], v[22:23], v[46:47] op_sel_hi:[1,0]
	v_pk_mul_f32 v[20:21], v[20:21], v[46:47] op_sel_hi:[1,0]
	v_pk_mul_f32 v[18:19], v[18:19], v[46:47] op_sel_hi:[1,0]
	v_pk_mul_f32 v[16:17], v[16:17], v[46:47] op_sel_hi:[1,0]
	v_pk_mul_f32 v[14:15], v[14:15], v[46:47] op_sel_hi:[1,0]
	v_pk_mul_f32 v[12:13], v[12:13], v[46:47] op_sel_hi:[1,0]
	v_pk_mul_f32 v[10:11], v[10:11], v[46:47] op_sel_hi:[1,0]
	v_pk_mul_f32 v[8:9], v[8:9], v[46:47] op_sel_hi:[1,0]
	v_pk_mul_f32 v[6:7], v[6:7], v[46:47] op_sel_hi:[1,0]
	v_pk_mul_f32 v[4:5], v[4:5], v[46:47] op_sel_hi:[1,0]
	v_mul_f32_e32 v175, v175, v46
	s_branch .LBB0_1310

; #define LAS __attribute__((address_space(3)))
;     DI void operator()(f32x4 (&acc)[2][2][4][2], const Unit& u, int wr, int wc, int fr, int fq, const LAS unsigned char* slot) const {
;     ...
;             for (int m = 0; m < 4; ++m) { const int lr = ai * HALF + wr * 64 + m * 16 + fr; gtv[ai][m] = *(const LAS float*)(slot + 4 * lr); rsv[ai][m] = *(const LAS float*)(slot + 1024 + 4 * lr); rmx[ai][m] = 0.f; }
; #pragma unroll
;         for (int bj = 0; bj < 2; ++bj) { float bv[8], cv[8];
;             { const int lc = bj * HALF + wc * 32 + 8 * fq; const f32x4 a = *(const LAS f32x4*)(slot + 2048 + 4 * lc), b = *(const LAS f32x4*)(slot + 2048 + 4 * lc + 16), c = *(const LAS f32x4*)(slot + 3072 + 4 * lc), d = *(const LAS f32x4*)(slot + 3072 + 4 * lc + 16);
; #pragma unroll
;               for (int j = 0; j < 4; ++j) { bv[j] = a[j]; bv[4 + j] = b[j]; cv[j] = c[j]; cv[4 + j] = d[j]; } }
; #pragma unroll
;             for (int ai = 0; ai < 2; ++ai)
; #pragma unroll
;                 for (int m = 0; m < 4; ++m) { const float gt = gtv[ai][m], rs = rsv[ai][m];
; #pragma unroll
;                     for (int n = 0; n < 2; ++n) { const i32x4 ia = __builtin_bit_cast(i32x4, acc[ai][bj][m][n]); f32x4 v;
; #pragma unroll
;                         for (int k = 0; k < 4; ++k) { v[k] = ((float)ia[k] * (rs * cv[4 * n + k]) + bv[4 * n + k]) * gt; rmx[ai][m] = fmaxf(rmx[ai][m], fabsf(v[k])); }
;                         acc[ai][bj][m][n] = v; } } }
;         LAS float* xch = (LAS float*)(slot + 8192);
; #pragma unroll
;         for (int ai = 0; ai < 2; ++ai)
; #pragma unroll
;             for (int m = 0; m < 4; ++m) { float x = rmx[ai][m]; x = fmaxf(x, __shfl_xor(x, 16)); x = fmaxf(x, __shfl_xor(x, 32));
;                 if (fq == 0) xch[(ai * HALF + wr * 64 + m * 16 + fr) * 4 + wc] = x; }
.LBB0_2454:
	s_lshl_b32 s38, s73, 12
	s_and_b32 s38, s38, 0x1000
	s_add_i32 s42, s38, 0
	s_add_i32 s42, s42, 0x21000
	v_add_u32_e32 v116, s42, v184
	v_mov_b32_e32 v203, v157
	v_add_u32_e32 v117, 0x400, v116
	v_add_u32_e32 v206, s42, v187
	ds_read2_b32 v[178:179], v116 offset1:16
	ds_read2_b32 v[180:181], v117 offset1:16
	ds_read2_b32 v[174:175], v116 offset0:32 offset1:48
	ds_read2_b32 v[176:177], v117 offset0:32 offset1:48
	ds_read2_b32 v[170:171], v116 offset0:128 offset1:144
	ds_read2_b32 v[172:173], v117 offset0:128 offset1:144
	ds_read2_b32 v[166:167], v116 offset0:160 offset1:176
	ds_read2_b32 v[168:169], v117 offset0:160 offset1:176
	ds_read_b128 v[140:143], v206 offset:3072
	ds_read_b128 v[136:139], v206 offset:2048
	ds_read_b128 v[116:119], v206 offset:2064
	v_cvt_f32_i32_e32 v132, v132
	v_cvt_f32_i32_e32 v133, v133
	s_waitcnt lgkmcnt(0)
	v_mul_f32_e32 v144, v180, v140
	v_cvt_f32_i32_e32 v135, v135
	v_fma_f32 v132, v144, v132, v136
	v_mul_f32_e32 v156, v178, v132
	v_mul_f32_e32 v132, v180, v141
	v_fma_f32 v132, v132, v133, v137
	v_mul_f32_e32 v198, v178, v132
	v_cvt_f32_i32_e32 v132, v134
	ds_read_b128 v[124:127], v206 offset:3088
	v_mul_f32_e32 v134, v180, v142
	v_cvt_f32_i32_e32 v120, v120
	v_fma_f32 v132, v134, v132, v138
	v_mul_f32_e32 v199, v178, v132
	v_mul_f32_e32 v132, v180, v143
	v_fma_f32 v132, v132, v135, v139
	v_max3_f32 v133, |v156|, 0, |v198|
	v_mul_f32_e32 v200, v178, v132
	v_cvt_f32_i32_e32 v121, v121
	v_max3_f32 v132, v133, |v199|, |v200|
	s_waitcnt lgkmcnt(0)
	v_mul_f32_e32 v133, v180, v124
	v_fma_f32 v120, v133, v120, v116
	v_mul_f32_e32 v201, v178, v120
	v_mul_f32_e32 v120, v180, v125
	v_fma_f32 v120, v120, v121, v117
	v_mul_f32_e32 v202, v178, v120
	v_cvt_f32_i32_e32 v120, v122
	v_cvt_f32_i32_e32 v123, v123
	v_mul_f32_e32 v122, v180, v126
	v_max3_f32 v121, v132, |v201|, |v202|
	v_fma_f32 v120, v122, v120, v118
	v_mul_f32_e32 v204, v178, v120
	v_mul_f32_e32 v120, v180, v127
	v_fma_f32 v120, v120, v123, v119
	v_mul_f32_e32 v205, v178, v120
	v_max3_f32 v207, v121, |v204|, |v205|
	ds_read_b128 v[148:151], v206 offset:3584
	ds_read_b128 v[144:147], v206 offset:2560
	ds_read_b128 v[120:123], v206 offset:2576
	v_cvt_f32_i32_e32 v128, v128
	v_cvt_f32_i32_e32 v129, v129
	ds_read_b128 v[132:135], v206 offset:3600
	s_waitcnt lgkmcnt(0)
	v_mul_f32_e32 v206, v180, v148
	v_fma_f32 v128, v206, v128, v144
	v_mul_f32_e32 v206, v180, v149
	v_cvt_f32_i32_e32 v130, v130
	v_fma_f32 v129, v206, v129, v145
	v_cvt_f32_i32_e32 v131, v131
	v_mul_f32_e32 v128, v178, v128
	v_mul_f32_e32 v129, v178, v129
	v_cvt_f32_i32_e32 v112, v112
	v_max3_f32 v206, v207, |v128|, |v129|
	v_mul_f32_e32 v207, v180, v150
	v_cvt_f32_i32_e32 v113, v113
	v_fma_f32 v130, v207, v130, v146
	v_mul_f32_e32 v207, v180, v151
	v_cvt_f32_i32_e32 v114, v114
	v_cvt_f32_i32_e32 v115, v115
	v_fma_f32 v131, v207, v131, v147
	v_mul_f32_e32 v207, v180, v132
	v_fma_f32 v112, v207, v112, v120
	v_mul_f32_e32 v207, v180, v133
	v_mul_f32_e32 v130, v178, v130
	v_mul_f32_e32 v131, v178, v131
	v_fma_f32 v113, v207, v113, v121
	v_mul_f32_e32 v207, v180, v134
	v_mul_f32_e32 v180, v180, v135
	v_max3_f32 v206, v206, |v130|, |v131|
	v_mul_f32_e32 v112, v178, v112
	v_mul_f32_e32 v113, v178, v113
	v_fma_f32 v114, v207, v114, v122
	v_fma_f32 v115, v180, v115, v123
	v_max3_f32 v206, v206, |v112|, |v113|
	v_mul_f32_e32 v114, v178, v114
	v_mul_f32_e32 v115, v178, v115
	v_max3_f32 v180, v206, |v114|, |v115|
	v_and_b32_e32 v206, 64, v193
	v_xor_b32_e32 v178, 16, v193
	v_add_u32_e32 v206, 64, v206
	v_cmp_lt_i32_e32 vcc, v178, v206
	v_xor_b32_e32 v208, 32, v193
	s_lshl_b32 s38, s69, 2
	v_cndmask_b32_e32 v178, v193, v178, vcc
	v_lshlrev_b32_e32 v178, 2, v178
	v_cmp_lt_i32_e32 vcc, v208, v206
	s_add_i32 s38, s42, s38
	v_mov_b32_e32 v207, v180
	v_cndmask_b32_e32 v206, v193, v208, vcc
	v_lshlrev_b32_e32 v206, 2, v206
	v_mov_b32_e32 v208, v180
	s_nop 1
	v_permlane16_swap_b32 v207, v208
	v_max_f32_e32 v207, v207, v208
	v_mov_b32_e32 v208, v207
	s_nop 1
	v_permlane32_swap_b32 v207, v208
	v_max_f32_e32 v207, v207, v208
	v_add_u32_e32 v180, s38, v188
	s_and_saveexec_b64 s[38:39], s[4:5]
	s_cbranch_execz .LBB0_2456
	ds_write_b32 v180, v207 offset:8192
.LBB0_2456:
	s_or_b64 exec, exec, s[38:39]
	v_cvt_f32_i32_e32 v109, v109
	v_cvt_f32_i32_e32 v110, v110
	v_cvt_f32_i32_e32 v111, v111
	s_waitcnt lgkmcnt(0)
	v_mul_f32_e32 v208, v181, v141
	v_cvt_f32_i32_e32 v104, v104
	v_fma_f32 v109, v208, v109, v137
	v_mul_f32_e32 v208, v181, v142
	v_cvt_f32_i32_e32 v105, v105
	v_fma_f32 v110, v208, v110, v138
	v_mul_f32_e32 v208, v181, v143
	v_cvt_f32_i32_e32 v106, v106
	v_cvt_f32_i32_e32 v108, v108
	v_fma_f32 v111, v208, v111, v139
	v_mul_f32_e32 v208, v181, v124
	v_cvt_f32_i32_e32 v107, v107
	v_fma_f32 v104, v208, v104, v116
	v_mul_f32_e32 v208, v181, v125
	v_cvt_f32_i32_e32 v100, v100
	v_fma_f32 v105, v208, v105, v117
	v_mul_f32_e32 v208, v181, v126
	v_cvt_f32_i32_e32 v101, v101
	v_mul_f32_e32 v207, v181, v140
	v_fma_f32 v106, v208, v106, v118
	v_mul_f32_e32 v208, v181, v127
	v_cvt_f32_i32_e32 v102, v102
	v_fma_f32 v108, v207, v108, v136
	v_fma_f32 v107, v208, v107, v119
	v_mul_f32_e32 v208, v181, v148
	v_cvt_f32_i32_e32 v103, v103
	v_mul_f32_e32 v108, v179, v108
	v_mul_f32_e32 v109, v179, v109
	v_fma_f32 v100, v208, v100, v144
	v_mul_f32_e32 v208, v181, v149
	v_cvt_f32_i32_e32 v96, v96
	v_max3_f32 v207, |v108|, 0, |v109|
	v_mul_f32_e32 v110, v179, v110
	v_mul_f32_e32 v111, v179, v111
	v_fma_f32 v101, v208, v101, v145
	v_mul_f32_e32 v208, v181, v150
	v_cvt_f32_i32_e32 v97, v97
	v_max3_f32 v207, v207, |v110|, |v111|
	v_mul_f32_e32 v104, v179, v104
	v_mul_f32_e32 v105, v179, v105
	v_fma_f32 v102, v208, v102, v146
	v_mul_f32_e32 v208, v181, v151
	v_cvt_f32_i32_e32 v98, v98
	v_cvt_f32_i32_e32 v99, v99
	v_max3_f32 v207, v207, |v104|, |v105|
	v_mul_f32_e32 v106, v179, v106
	v_mul_f32_e32 v107, v179, v107
	v_fma_f32 v103, v208, v103, v147
	v_mul_f32_e32 v208, v181, v132
	v_max3_f32 v207, v207, |v106|, |v107|
	v_mul_f32_e32 v100, v179, v100
	v_mul_f32_e32 v101, v179, v101
	v_fma_f32 v96, v208, v96, v120
	v_mul_f32_e32 v208, v181, v133
	v_max3_f32 v207, v207, |v100|, |v101|
	v_mul_f32_e32 v102, v179, v102
	v_mul_f32_e32 v103, v179, v103
	v_fma_f32 v97, v208, v97, v121
	v_mul_f32_e32 v208, v181, v134
	v_mul_f32_e32 v181, v181, v135
	v_max3_f32 v207, v207, |v102|, |v103|
	v_mul_f32_e32 v96, v179, v96
	v_mul_f32_e32 v97, v179, v97
	v_fma_f32 v98, v208, v98, v122
	v_fma_f32 v99, v181, v99, v123
	v_max3_f32 v207, v207, |v96|, |v97|
	v_mul_f32_e32 v98, v179, v98
	v_mul_f32_e32 v99, v179, v99
	v_max3_f32 v179, v207, |v98|, |v99|
	v_mov_b32_e32 v181, v179
	s_nop 1
	v_permlane16_swap_b32 v179, v181
	v_max_f32_e32 v179, v179, v181
	v_mov_b32_e32 v181, v179
	s_nop 1
	v_permlane32_swap_b32 v179, v181
	v_max_f32_e32 v179, v179, v181
	s_and_saveexec_b64 s[38:39], s[4:5]
	s_cbranch_execz .LBB0_2458
	ds_write_b32 v180, v179 offset:8448
; #define LAS __attribute__((address_space(3)))
;     DI void operator()(f32x4 (&acc)[2][2][4][2], const Unit& u, int wr, int wc, int fr, int fq, const LAS unsigned char* slot) const {
;     ...
;                 for (int m = 0; m < 4; ++m) { const float gt = gtv[ai][m], rs = rsv[ai][m];
; #pragma unroll
;                     for (int n = 0; n < 2; ++n) { const i32x4 ia = __builtin_bit_cast(i32x4, acc[ai][bj][m][n]); f32x4 v;
; #pragma unroll
;                         for (int k = 0; k < 4; ++k) { v[k] = ((float)ia[k] * (rs * cv[4 * n + k]) + bv[4 * n + k]) * gt; rmx[ai][m] = fmaxf(rmx[ai][m], fabsf(v[k])); }
;                         acc[ai][bj][m][n] = v; } } }
;         LAS float* xch = (LAS float*)(slot + 8192);
; #pragma unroll
;         for (int ai = 0; ai < 2; ++ai)
; #pragma unroll
;             for (int m = 0; m < 4; ++m) { float x = rmx[ai][m]; x = fmaxf(x, __shfl_xor(x, 16)); x = fmaxf(x, __shfl_xor(x, 32));
;                 if (fq == 0) xch[(ai * HALF + wr * 64 + m * 16 + fr) * 4 + wc] = x; }
.LBB0_2458:
	s_or_b64 exec, exec, s[38:39]
	v_cvt_f32_i32_e32 v93, v93
	v_cvt_f32_i32_e32 v94, v94
	v_cvt_f32_i32_e32 v95, v95
	s_waitcnt lgkmcnt(0)
	v_mul_f32_e32 v181, v176, v141
	v_cvt_f32_i32_e32 v88, v88
	v_fma_f32 v93, v181, v93, v137
	v_mul_f32_e32 v181, v176, v142
	v_cvt_f32_i32_e32 v89, v89
	v_fma_f32 v94, v181, v94, v138
	v_mul_f32_e32 v181, v176, v143
	v_cvt_f32_i32_e32 v90, v90
	v_cvt_f32_i32_e32 v92, v92
	v_fma_f32 v95, v181, v95, v139
	v_mul_f32_e32 v181, v176, v124
	v_cvt_f32_i32_e32 v91, v91
	v_fma_f32 v88, v181, v88, v116
	v_mul_f32_e32 v181, v176, v125
	v_cvt_f32_i32_e32 v84, v84
	v_fma_f32 v89, v181, v89, v117
	v_mul_f32_e32 v181, v176, v126
	v_cvt_f32_i32_e32 v85, v85
	v_mul_f32_e32 v179, v176, v140
	v_fma_f32 v90, v181, v90, v118
	v_mul_f32_e32 v181, v176, v127
	v_cvt_f32_i32_e32 v86, v86
	v_fma_f32 v92, v179, v92, v136
	v_fma_f32 v91, v181, v91, v119
	v_mul_f32_e32 v181, v176, v148
	v_cvt_f32_i32_e32 v87, v87
	v_mul_f32_e32 v92, v174, v92
	v_mul_f32_e32 v93, v174, v93
	v_fma_f32 v84, v181, v84, v144
	v_mul_f32_e32 v181, v176, v149
	v_cvt_f32_i32_e32 v80, v80
	v_max3_f32 v179, |v92|, 0, |v93|
	v_mul_f32_e32 v94, v174, v94
	v_mul_f32_e32 v95, v174, v95
	v_fma_f32 v85, v181, v85, v145
	v_mul_f32_e32 v181, v176, v150
	v_cvt_f32_i32_e32 v81, v81
	v_max3_f32 v179, v179, |v94|, |v95|
	v_mul_f32_e32 v88, v174, v88
	v_mul_f32_e32 v89, v174, v89
	v_fma_f32 v86, v181, v86, v146
	v_mul_f32_e32 v181, v176, v151
	v_cvt_f32_i32_e32 v82, v82
	v_cvt_f32_i32_e32 v83, v83
	v_max3_f32 v179, v179, |v88|, |v89|
	v_mul_f32_e32 v90, v174, v90
	v_mul_f32_e32 v91, v174, v91
	v_fma_f32 v87, v181, v87, v147
	v_mul_f32_e32 v181, v176, v132
	v_max3_f32 v179, v179, |v90|, |v91|
	v_mul_f32_e32 v84, v174, v84
	v_mul_f32_e32 v85, v174, v85
	v_fma_f32 v80, v181, v80, v120
	v_mul_f32_e32 v181, v176, v133
	v_max3_f32 v179, v179, |v84|, |v85|
	v_mul_f32_e32 v86, v174, v86
	v_mul_f32_e32 v87, v174, v87
	v_fma_f32 v81, v181, v81, v121
	v_mul_f32_e32 v181, v176, v134
	v_mul_f32_e32 v176, v176, v135
	v_max3_f32 v179, v179, |v86|, |v87|
	v_mul_f32_e32 v80, v174, v80
	v_mul_f32_e32 v81, v174, v81
	v_fma_f32 v82, v181, v82, v122
	v_fma_f32 v83, v176, v83, v123
	v_max3_f32 v179, v179, |v80|, |v81|
	v_mul_f32_e32 v82, v174, v82
	v_mul_f32_e32 v83, v174, v83
	v_max3_f32 v174, v179, |v82|, |v83|
	v_mov_b32_e32 v176, v174
	s_nop 1
	v_permlane16_swap_b32 v174, v176
	v_max_f32_e32 v174, v174, v176
	v_mov_b32_e32 v176, v174
	s_nop 1
	v_permlane32_swap_b32 v174, v176
	v_max_f32_e32 v174, v174, v176
	s_and_saveexec_b64 s[38:39], s[4:5]
	s_cbranch_execz .LBB0_2460
	ds_write_b32 v180, v174 offset:8704
.LBB0_2460:
	s_or_b64 exec, exec, s[38:39]
	v_cvt_f32_i32_e32 v77, v77
	v_cvt_f32_i32_e32 v78, v78
	v_cvt_f32_i32_e32 v79, v79
	s_waitcnt lgkmcnt(0)
	v_mul_f32_e32 v176, v177, v141
	v_cvt_f32_i32_e32 v72, v72
	v_fma_f32 v77, v176, v77, v137
	v_mul_f32_e32 v176, v177, v142
	v_cvt_f32_i32_e32 v73, v73
	v_fma_f32 v78, v176, v78, v138
	v_mul_f32_e32 v176, v177, v143
	v_cvt_f32_i32_e32 v74, v74
	v_fma_f32 v79, v176, v79, v139
	v_mul_f32_e32 v176, v177, v124
	v_cvt_f32_i32_e32 v75, v75
	v_cvt_f32_i32_e32 v76, v76
	v_fma_f32 v72, v176, v72, v116
	v_mul_f32_e32 v176, v177, v125
	v_cvt_f32_i32_e32 v68, v68
	v_fma_f32 v73, v176, v73, v117
	v_mul_f32_e32 v176, v177, v126
	v_cvt_f32_i32_e32 v69, v69
	v_fma_f32 v74, v176, v74, v118
	v_mul_f32_e32 v176, v177, v127
	v_cvt_f32_i32_e32 v70, v70
	v_mul_f32_e32 v174, v177, v140
	v_fma_f32 v75, v176, v75, v119
	v_mul_f32_e32 v176, v177, v148
	v_cvt_f32_i32_e32 v71, v71
	v_fma_f32 v76, v174, v76, v136
	v_fma_f32 v68, v176, v68, v144
	v_mul_f32_e32 v176, v177, v149
	v_cvt_f32_i32_e32 v64, v64
	v_mul_f32_e32 v76, v175, v76
	v_mul_f32_e32 v77, v175, v77
	v_fma_f32 v69, v176, v69, v145
	v_mul_f32_e32 v176, v177, v150
	v_cvt_f32_i32_e32 v65, v65
	v_max3_f32 v174, |v76|, 0, |v77|
	v_mul_f32_e32 v78, v175, v78
	v_mul_f32_e32 v79, v175, v79
	v_fma_f32 v70, v176, v70, v146
	v_mul_f32_e32 v176, v177, v151
	v_cvt_f32_i32_e32 v66, v66
	v_max3_f32 v174, v174, |v78|, |v79|
	v_mul_f32_e32 v72, v175, v72
	v_mul_f32_e32 v73, v175, v73
	v_fma_f32 v71, v176, v71, v147
	v_mul_f32_e32 v176, v177, v132
	v_cvt_f32_i32_e32 v67, v67
	v_max3_f32 v174, v174, |v72|, |v73|
	v_mul_f32_e32 v74, v175, v74
	v_mul_f32_e32 v75, v175, v75
	v_fma_f32 v64, v176, v64, v120
	v_mul_f32_e32 v176, v177, v133
	v_max3_f32 v174, v174, |v74|, |v75|
	v_mul_f32_e32 v68, v175, v68
	v_mul_f32_e32 v69, v175, v69
	v_fma_f32 v65, v176, v65, v121
	v_mul_f32_e32 v176, v177, v134
	v_max3_f32 v174, v174, |v68|, |v69|
	v_mul_f32_e32 v70, v175, v70
	v_mul_f32_e32 v71, v175, v71
	v_fma_f32 v66, v176, v66, v122
	v_mul_f32_e32 v176, v177, v135
	v_max3_f32 v174, v174, |v70|, |v71|
	v_mul_f32_e32 v64, v175, v64
	v_mul_f32_e32 v65, v175, v65
	v_fma_f32 v67, v176, v67, v123
	v_max3_f32 v174, v174, |v64|, |v65|
	v_mul_f32_e32 v66, v175, v66
	v_mul_f32_e32 v67, v175, v67
	v_max3_f32 v174, v174, |v66|, |v67|
	v_mov_b32_e32 v175, v174
	s_nop 1
	v_permlane16_swap_b32 v174, v175
	v_max_f32_e32 v174, v174, v175
	v_mov_b32_e32 v175, v174
	s_nop 1
	v_permlane32_swap_b32 v174, v175
	v_max_f32_e32 v174, v174, v175
	s_and_saveexec_b64 s[38:39], s[4:5]
	s_cbranch_execz .LBB0_2462
	ds_write_b32 v180, v174 offset:8960
; #define LAS __attribute__((address_space(3)))
;     DI void operator()(f32x4 (&acc)[2][2][4][2], const Unit& u, int wr, int wc, int fr, int fq, const LAS unsigned char* slot) const {
;     ...
;                 for (int m = 0; m < 4; ++m) { const float gt = gtv[ai][m], rs = rsv[ai][m];
; #pragma unroll
;                     for (int n = 0; n < 2; ++n) { const i32x4 ia = __builtin_bit_cast(i32x4, acc[ai][bj][m][n]); f32x4 v;
; #pragma unroll
;                         for (int k = 0; k < 4; ++k) { v[k] = ((float)ia[k] * (rs * cv[4 * n + k]) + bv[4 * n + k]) * gt; rmx[ai][m] = fmaxf(rmx[ai][m], fabsf(v[k])); }
;                         acc[ai][bj][m][n] = v; } } }
;         LAS float* xch = (LAS float*)(slot + 8192);
; #pragma unroll
;         for (int ai = 0; ai < 2; ++ai)
; #pragma unroll
;             for (int m = 0; m < 4; ++m) { float x = rmx[ai][m]; x = fmaxf(x, __shfl_xor(x, 16)); x = fmaxf(x, __shfl_xor(x, 32));
;                 if (fq == 0) xch[(ai * HALF + wr * 64 + m * 16 + fr) * 4 + wc] = x; }
.LBB0_2462:
	s_or_b64 exec, exec, s[38:39]
	v_cvt_f32_i32_e32 v61, v61
	v_cvt_f32_i32_e32 v62, v62
	v_cvt_f32_i32_e32 v63, v63
	s_waitcnt lgkmcnt(0)
	v_mul_f32_e32 v175, v172, v141
	v_cvt_f32_i32_e32 v56, v56
	v_fma_f32 v61, v175, v61, v137
	v_mul_f32_e32 v175, v172, v142
	v_cvt_f32_i32_e32 v57, v57
	v_fma_f32 v62, v175, v62, v138
	v_mul_f32_e32 v175, v172, v143
	v_cvt_f32_i32_e32 v58, v58
	v_cvt_f32_i32_e32 v60, v60
	v_fma_f32 v63, v175, v63, v139
	v_mul_f32_e32 v175, v172, v124
	v_cvt_f32_i32_e32 v59, v59
	v_fma_f32 v56, v175, v56, v116
	v_mul_f32_e32 v175, v172, v125
	v_cvt_f32_i32_e32 v52, v52
	v_fma_f32 v57, v175, v57, v117
	v_mul_f32_e32 v175, v172, v126
	v_cvt_f32_i32_e32 v53, v53
	v_mul_f32_e32 v174, v172, v140
	v_fma_f32 v58, v175, v58, v118
	v_mul_f32_e32 v175, v172, v127
	v_cvt_f32_i32_e32 v54, v54
	v_fma_f32 v60, v174, v60, v136
	v_fma_f32 v59, v175, v59, v119
	v_mul_f32_e32 v175, v172, v148
	v_cvt_f32_i32_e32 v55, v55
	v_mul_f32_e32 v60, v170, v60
	v_mul_f32_e32 v61, v170, v61
	v_fma_f32 v52, v175, v52, v144
	v_mul_f32_e32 v175, v172, v149
	v_cvt_f32_i32_e32 v48, v48
	v_max3_f32 v174, |v60|, 0, |v61|
	v_mul_f32_e32 v62, v170, v62
	v_mul_f32_e32 v63, v170, v63
	v_fma_f32 v53, v175, v53, v145
	v_mul_f32_e32 v175, v172, v150
	v_cvt_f32_i32_e32 v49, v49
	v_max3_f32 v174, v174, |v62|, |v63|
	v_mul_f32_e32 v56, v170, v56
	v_mul_f32_e32 v57, v170, v57
	v_fma_f32 v54, v175, v54, v146
	v_mul_f32_e32 v175, v172, v151
	v_cvt_f32_i32_e32 v50, v50
	v_cvt_f32_i32_e32 v51, v51
	v_max3_f32 v174, v174, |v56|, |v57|
	v_mul_f32_e32 v58, v170, v58
	v_mul_f32_e32 v59, v170, v59
	v_fma_f32 v55, v175, v55, v147
	v_mul_f32_e32 v175, v172, v132
	v_max3_f32 v174, v174, |v58|, |v59|
	v_mul_f32_e32 v52, v170, v52
	v_mul_f32_e32 v53, v170, v53
	v_fma_f32 v48, v175, v48, v120
	v_mul_f32_e32 v175, v172, v133
	v_max3_f32 v174, v174, |v52|, |v53|
	v_mul_f32_e32 v54, v170, v54
	v_mul_f32_e32 v55, v170, v55
	v_fma_f32 v49, v175, v49, v121
	v_mul_f32_e32 v175, v172, v134
	v_mul_f32_e32 v172, v172, v135
	v_max3_f32 v174, v174, |v54|, |v55|
	v_mul_f32_e32 v48, v170, v48
	v_mul_f32_e32 v49, v170, v49
	v_fma_f32 v50, v175, v50, v122
	v_fma_f32 v51, v172, v51, v123
	v_max3_f32 v174, v174, |v48|, |v49|
	v_mul_f32_e32 v50, v170, v50
	v_mul_f32_e32 v51, v170, v51
	v_max3_f32 v170, v174, |v50|, |v51|
	v_mov_b32_e32 v172, v170
	s_nop 1
	v_permlane16_swap_b32 v170, v172
	v_max_f32_e32 v170, v170, v172
	v_mov_b32_e32 v172, v170
	s_nop 1
	v_permlane32_swap_b32 v170, v172
	v_max_f32_e32 v170, v170, v172
	s_and_saveexec_b64 s[38:39], s[4:5]
	s_cbranch_execz .LBB0_2464
	ds_write_b32 v180, v170 offset:10240
.LBB0_2464:
	s_or_b64 exec, exec, s[38:39]
	v_cvt_f32_i32_e32 v45, v45
	v_cvt_f32_i32_e32 v46, v46
	v_cvt_f32_i32_e32 v47, v47
	s_waitcnt lgkmcnt(0)
	v_mul_f32_e32 v172, v173, v141
	v_cvt_f32_i32_e32 v40, v40
	v_fma_f32 v45, v172, v45, v137
	v_mul_f32_e32 v172, v173, v142
	v_cvt_f32_i32_e32 v41, v41
	v_fma_f32 v46, v172, v46, v138
	v_mul_f32_e32 v172, v173, v143
	v_cvt_f32_i32_e32 v42, v42
	v_fma_f32 v47, v172, v47, v139
	v_mul_f32_e32 v172, v173, v124
	v_cvt_f32_i32_e32 v43, v43
	v_cvt_f32_i32_e32 v44, v44
	v_fma_f32 v40, v172, v40, v116
	v_mul_f32_e32 v172, v173, v125
	v_cvt_f32_i32_e32 v36, v36
	v_fma_f32 v41, v172, v41, v117
	v_mul_f32_e32 v172, v173, v126
	v_cvt_f32_i32_e32 v37, v37
	v_fma_f32 v42, v172, v42, v118
	v_mul_f32_e32 v172, v173, v127
	v_cvt_f32_i32_e32 v38, v38
	v_mul_f32_e32 v170, v173, v140
	v_fma_f32 v43, v172, v43, v119
	v_mul_f32_e32 v172, v173, v148
	v_cvt_f32_i32_e32 v39, v39
	v_fma_f32 v44, v170, v44, v136
	v_fma_f32 v36, v172, v36, v144
	v_mul_f32_e32 v172, v173, v149
	v_cvt_f32_i32_e32 v24, v24
	v_mul_f32_e32 v44, v171, v44
	v_mul_f32_e32 v45, v171, v45
	v_fma_f32 v37, v172, v37, v145
	v_mul_f32_e32 v172, v173, v150
	v_cvt_f32_i32_e32 v25, v25
	v_max3_f32 v170, |v44|, 0, |v45|
	v_mul_f32_e32 v46, v171, v46
	v_mul_f32_e32 v47, v171, v47
	v_fma_f32 v38, v172, v38, v146
	v_mul_f32_e32 v172, v173, v151
	v_cvt_f32_i32_e32 v26, v26
	v_max3_f32 v170, v170, |v46|, |v47|
	v_mul_f32_e32 v40, v171, v40
	v_mul_f32_e32 v41, v171, v41
	v_fma_f32 v39, v172, v39, v147
	v_mul_f32_e32 v172, v173, v132
	v_cvt_f32_i32_e32 v27, v27
	v_max3_f32 v170, v170, |v40|, |v41|
	v_mul_f32_e32 v42, v171, v42
	v_mul_f32_e32 v43, v171, v43
	v_fma_f32 v24, v172, v24, v120
	v_mul_f32_e32 v172, v173, v133
	v_max3_f32 v170, v170, |v42|, |v43|
	v_mul_f32_e32 v36, v171, v36
	v_mul_f32_e32 v37, v171, v37
	v_fma_f32 v25, v172, v25, v121
	v_mul_f32_e32 v172, v173, v134
	v_max3_f32 v170, v170, |v36|, |v37|
	v_mul_f32_e32 v38, v171, v38
	v_mul_f32_e32 v39, v171, v39
	v_fma_f32 v26, v172, v26, v122
	v_mul_f32_e32 v172, v173, v135
	v_max3_f32 v170, v170, |v38|, |v39|
	v_mul_f32_e32 v24, v171, v24
	v_mul_f32_e32 v25, v171, v25
	v_fma_f32 v27, v172, v27, v123
	v_max3_f32 v170, v170, |v24|, |v25|
	v_mul_f32_e32 v26, v171, v26
	v_mul_f32_e32 v27, v171, v27
	v_max3_f32 v170, v170, |v26|, |v27|
	v_mov_b32_e32 v171, v170
	s_nop 1
	v_permlane16_swap_b32 v170, v171
	v_max_f32_e32 v170, v170, v171
	v_mov_b32_e32 v171, v170
	s_nop 1
	v_permlane32_swap_b32 v170, v171
	v_max_f32_e32 v170, v170, v171
	s_and_saveexec_b64 s[38:39], s[4:5]
	s_cbranch_execz .LBB0_2466
	ds_write_b32 v180, v170 offset:10496
; #define LAS __attribute__((address_space(3)))
;     DI void operator()(f32x4 (&acc)[2][2][4][2], const Unit& u, int wr, int wc, int fr, int fq, const LAS unsigned char* slot) const {
;     ...
;                 for (int m = 0; m < 4; ++m) { const float gt = gtv[ai][m], rs = rsv[ai][m];
; #pragma unroll
;                     for (int n = 0; n < 2; ++n) { const i32x4 ia = __builtin_bit_cast(i32x4, acc[ai][bj][m][n]); f32x4 v;
; #pragma unroll
;                         for (int k = 0; k < 4; ++k) { v[k] = ((float)ia[k] * (rs * cv[4 * n + k]) + bv[4 * n + k]) * gt; rmx[ai][m] = fmaxf(rmx[ai][m], fabsf(v[k])); }
;                         acc[ai][bj][m][n] = v; } } }
;         LAS float* xch = (LAS float*)(slot + 8192);
; #pragma unroll
;         for (int ai = 0; ai < 2; ++ai)
; #pragma unroll
;             for (int m = 0; m < 4; ++m) { float x = rmx[ai][m]; x = fmaxf(x, __shfl_xor(x, 16)); x = fmaxf(x, __shfl_xor(x, 32));
;                 if (fq == 0) xch[(ai * HALF + wr * 64 + m * 16 + fr) * 4 + wc] = x; }
.LBB0_2466:
	s_or_b64 exec, exec, s[38:39]
	v_cvt_f32_i32_e32 v21, v21
	v_cvt_f32_i32_e32 v22, v22
	v_cvt_f32_i32_e32 v23, v23
	s_waitcnt lgkmcnt(0)
	v_mul_f32_e32 v171, v168, v141
	v_cvt_f32_i32_e32 v16, v16
	v_fma_f32 v21, v171, v21, v137
	v_mul_f32_e32 v171, v168, v142
	v_cvt_f32_i32_e32 v17, v17
	v_cvt_f32_i32_e32 v20, v20
	v_fma_f32 v22, v171, v22, v138
	v_mul_f32_e32 v171, v168, v143
	v_cvt_f32_i32_e32 v18, v18
	v_fma_f32 v23, v171, v23, v139
	v_mul_f32_e32 v171, v168, v124
	v_cvt_f32_i32_e32 v19, v19
	v_fma_f32 v16, v171, v16, v116
	v_mul_f32_e32 v171, v168, v125
	v_cvt_f32_i32_e32 v32, v32
	v_mul_f32_e32 v170, v168, v140
	v_fma_f32 v17, v171, v17, v117
	v_mul_f32_e32 v171, v168, v126
	v_cvt_f32_i32_e32 v33, v33
	v_fma_f32 v20, v170, v20, v136
	v_fma_f32 v18, v171, v18, v118
	v_mul_f32_e32 v171, v168, v127
	v_cvt_f32_i32_e32 v34, v34
	v_mul_f32_e32 v20, v166, v20
	v_mul_f32_e32 v21, v166, v21
	v_fma_f32 v19, v171, v19, v119
	v_mul_f32_e32 v171, v168, v148
	v_cvt_f32_i32_e32 v35, v35
	v_max3_f32 v170, |v20|, 0, |v21|
	v_mul_f32_e32 v22, v166, v22
	v_mul_f32_e32 v23, v166, v23
	v_fma_f32 v32, v171, v32, v144
	v_mul_f32_e32 v171, v168, v149
	v_max3_f32 v170, v170, |v22|, |v23|
	v_mul_f32_e32 v16, v166, v16
	v_mul_f32_e32 v17, v166, v17
	v_fma_f32 v33, v171, v33, v145
	v_mul_f32_e32 v171, v168, v150
	v_max3_f32 v170, v170, |v16|, |v17|
	v_mul_f32_e32 v18, v166, v18
	v_mul_f32_e32 v19, v166, v19
	v_fma_f32 v34, v171, v34, v146
	v_mul_f32_e32 v171, v168, v151
	v_cvt_f32_i32_e32 v28, v28
	v_max3_f32 v170, v170, |v18|, |v19|
	v_mul_f32_e32 v32, v166, v32
	v_mul_f32_e32 v33, v166, v33
	v_fma_f32 v35, v171, v35, v147
	v_max3_f32 v170, v170, |v32|, |v33|
	v_mul_f32_e32 v34, v166, v34
	v_mul_f32_e32 v35, v166, v35
	v_cvt_f32_i32_e32 v29, v29
	v_max3_f32 v172, v170, |v34|, |v35|
	v_mul_f32_e32 v170, v168, v132
	v_fma_f32 v28, v170, v28, v120
	v_mul_f32_e32 v170, v166, v28
	v_mul_f32_e32 v28, v168, v133
	v_fma_f32 v28, v28, v29, v121
	v_mul_f32_e32 v171, v166, v28
	v_cvt_f32_i32_e32 v28, v30
	v_cvt_f32_i32_e32 v31, v31
	v_mul_f32_e32 v30, v168, v134
	v_max3_f32 v29, v172, |v170|, |v171|
	v_fma_f32 v28, v30, v28, v122
	v_mul_f32_e32 v172, v166, v28
	v_mul_f32_e32 v28, v168, v135
	v_fma_f32 v28, v28, v31, v123
	v_mul_f32_e32 v166, v166, v28
	v_max3_f32 v28, v29, |v172|, |v166|
	v_mov_b32_e32 v29, v28
	s_nop 1
	v_permlane16_swap_b32 v28, v29
	v_max_f32_e32 v28, v28, v29
	v_mov_b32_e32 v29, v28
	s_nop 1
	v_permlane32_swap_b32 v28, v29
	v_max_f32_e32 v28, v28, v29
	s_and_saveexec_b64 s[38:39], s[4:5]
	s_cbranch_execz .LBB0_2468
	ds_write_b32 v180, v28 offset:10752
.LBB0_2468:
	s_or_b64 exec, exec, s[38:39]
	v_cvt_f32_i32_e32 v4, v4
	v_cvt_f32_i32_e32 v5, v5
	v_mul_f32_e32 v28, v169, v140
	s_waitcnt lgkmcnt(0)
	v_mul_f32_e32 v29, v169, v141
	v_fma_f32 v4, v28, v4, v136
	v_mul_f32_e32 v28, v167, v4
	v_fma_f32 v4, v29, v5, v137
	v_mul_f32_e32 v29, v167, v4
	v_cvt_f32_i32_e32 v4, v6
	v_cvt_f32_i32_e32 v7, v7
	v_mul_f32_e32 v6, v169, v142
	v_cvt_f32_i32_e32 v0, v0
	v_fma_f32 v4, v6, v4, v138
	v_mul_f32_e32 v6, v167, v4
	v_mul_f32_e32 v4, v169, v143
	v_fmac_f32_e32 v139, v4, v7
	v_max3_f32 v5, |v28|, 0, |v29|
	v_mul_f32_e32 v7, v167, v139
	v_cvt_f32_i32_e32 v1, v1
	v_max3_f32 v4, v5, |v6|, |v7|
	v_mul_f32_e32 v5, v169, v124
	v_fma_f32 v0, v5, v0, v116
	v_mul_f32_e32 v30, v167, v0
	v_mul_f32_e32 v0, v169, v125
	v_fma_f32 v0, v0, v1, v117
	v_mul_f32_e32 v31, v167, v0
	v_cvt_f32_i32_e32 v0, v2
	v_cvt_f32_i32_e32 v3, v3
	v_mul_f32_e32 v2, v169, v126
	v_max3_f32 v1, v4, |v30|, |v31|
	v_fma_f32 v0, v2, v0, v118
	v_mul_f32_e32 v116, v167, v0
	v_mul_f32_e32 v0, v169, v127
	v_fmac_f32_e32 v119, v0, v3
	v_cvt_f32_i32_e32 v0, v12
	v_cvt_f32_i32_e32 v3, v13
	v_mul_f32_e32 v2, v169, v148
	v_mul_f32_e32 v117, v167, v119
	v_fma_f32 v0, v2, v0, v144
	v_mul_f32_e32 v12, v167, v0
	v_mul_f32_e32 v0, v169, v149
	v_fma_f32 v0, v0, v3, v145
	v_mul_f32_e32 v13, v167, v0
	v_cvt_f32_i32_e32 v0, v14
	v_cvt_f32_i32_e32 v3, v15
	v_mul_f32_e32 v2, v169, v150
	v_max3_f32 v1, v1, |v116|, |v117|
	v_fma_f32 v0, v2, v0, v146
	v_mul_f32_e32 v14, v167, v0
	v_mul_f32_e32 v0, v169, v151
	v_fmac_f32_e32 v147, v0, v3
	v_cvt_f32_i32_e32 v0, v8
	v_cvt_f32_i32_e32 v3, v9
	v_mul_f32_e32 v2, v169, v132
	v_max3_f32 v1, v1, |v12|, |v13|
	v_fma_f32 v0, v2, v0, v120
	v_mul_f32_e32 v8, v167, v0
	v_mul_f32_e32 v0, v169, v133
	v_fma_f32 v0, v0, v3, v121
	v_mul_f32_e32 v9, v167, v0
	v_cvt_f32_i32_e32 v0, v10
	v_cvt_f32_i32_e32 v3, v11
	v_mul_f32_e32 v2, v169, v134
	v_mul_f32_e32 v15, v167, v147
	v_fma_f32 v0, v2, v0, v122
	v_mul_f32_e32 v10, v167, v0
	v_mul_f32_e32 v0, v169, v135
	v_max3_f32 v1, v1, |v14|, |v15|
	v_fmac_f32_e32 v123, v0, v3
	v_max3_f32 v1, v1, |v8|, |v9|
	v_mul_f32_e32 v11, v167, v123
	v_max3_f32 v0, v1, |v10|, |v11|
	v_mov_b32_e32 v1, v0
	s_nop 1
	v_permlane16_swap_b32 v0, v1
	v_max_f32_e32 v0, v0, v1
	v_mov_b32_e32 v1, v0
	s_nop 1
	v_permlane32_swap_b32 v0, v1
	v_max_f32_e32 v0, v0, v1
	s_and_saveexec_b64 s[38:39], s[4:5]
	s_cbranch_execz .LBB0_2470
	ds_write_b32 v180, v0 offset:11008
